# on top of the XCD-contiguous MoE order: non-temporal (nt) policy on the expert-weight conversion loads and stores in phases 9, 11 and 13 (pure one-pass streams)
# speedup vs baseline: 1.0143x; 1.0013x over previous
.LBB0_770:
	s_ashr_i32 s5, s53, 31
	s_lshr_b32 s5, s5, 18
	s_add_i32 s5, s53, s5
	s_ashr_i32 s15, s5, 14
	s_and_b32 s5, s5, 0xffffc000
	s_sub_i32 s5, s53, s5
	s_sext_i32_i16 s25, s5
	s_lshr_b32 s25, s25, 22
	s_and_b32 s25, s25, 0x1ff
	s_add_i32 s25, s5, s25
	s_sext_i32_i16 s29, s25
	s_and_b32 s25, s25, 0xfe00
	s_sub_i32 s5, s5, s25
	s_sext_i32_i16 s25, s5
	s_bfe_u32 s25, s25, 0x4001b
	s_add_i32 s25, s5, s25
	s_lshr_b32 s34, s29, 9
	s_sext_i32_i16 s29, s25
	s_and_b32 s25, s25, 0xfff0
	s_sub_i32 s5, s5, s25
	s_sext_i32_i16 s5, s5
	s_lshl_b32 s56, s5, 5
	s_add_i32 s25, s53, 0x3fff
	s_cmpk_lt_u32 s25, 0x7fff
	s_cselect_b32 s25, s48, s50
	s_cselect_b32 s37, s47, s49
	s_bfe_i64 s[34:35], s[34:35], 0x100000
	s_lshl_b64 s[34:35], s[34:35], 22
	s_add_u32 s64, s37, s34
	s_addc_u32 s65, s25, s35
	s_add_u32 s38, s43, s34
	s_addc_u32 s39, s44, s35
	s_lshl_b32 s5, s5, 6
	s_and_b32 s25, s56, 0x60
	s_lshl_b32 s15, s15, 7
	s_and_b32 s5, s5, 0xffffff00
	s_or_b32 s15, s25, s15
	s_add_i32 s15, s15, s5
	s_lshl_b32 s5, s29, 2
	s_and_b32 s34, s5, 0xffffffc0
	v_or_b32_e32 v2, s34, v52
	v_ashrrev_i32_e32 v3, 31, v2
	v_lshlrev_b64 v[2:3], 11, v[2:3]
	v_lshl_add_u64 v[2:3], s[64:65], 0, v[2:3]
	s_ashr_i32 s57, s56, 31
	v_lshl_add_u64 v[2:3], s[56:57], 2, v[2:3]
	v_lshlrev_b32_e32 v34, 2, v54
	v_lshl_add_u64 v[2:3], v[2:3], 0, v[34:35]
	v_add_co_u32_e32 v4, vcc, s73, v2
	global_load_dwordx4 v[30:33], v[2:3], off nt
	global_load_dwordx4 v[36:39], v[2:3], off offset:2048 nt
	v_addc_co_u32_e32 v5, vcc, 0, v3, vcc
	v_add_co_u32_e32 v6, vcc, s90, v2
	v_or_b32_e32 v1, s24, v52
	s_nop 0
	v_addc_co_u32_e32 v7, vcc, 0, v3, vcc
	v_add_co_u32_e32 v2, vcc, s91, v2
	global_load_dwordx4 v[44:47], v[6:7], off offset:-4096 nt
	global_load_dwordx4 v[48:51], v[4:5], off offset:2048 nt
	global_load_dwordx4 v[56:59], v[6:7], off nt
	global_load_dwordx4 v[60:63], v[6:7], off offset:2048 nt
	v_addc_co_u32_e32 v3, vcc, 0, v3, vcc
	global_load_dwordx4 v[64:67], v[2:3], off nt
	global_load_dwordx4 v[68:71], v[2:3], off offset:2048 nt
	v_mul_hi_i32_i24_e32 v3, s36, v1
	v_mul_i32_i24_e32 v2, s36, v1
	v_lshl_add_u64 v[2:3], v[2:3], 2, s[30:31]
	s_ashr_i32 s5, s4, 31
	v_lshl_add_u64 v[2:3], s[4:5], 2, v[2:3]
	v_lshl_add_u64 v[6:7], v[2:3], 0, v[34:35]
	s_lshl_b32 s96, s36, 2
	v_lshl_add_u64 v[10:11], v[6:7], 0, s[96:97]
	v_lshl_add_u64 v[14:15], v[10:11], 0, s[96:97]
	v_lshl_add_u64 v[18:19], v[14:15], 0, s[96:97]
	v_lshl_add_u64 v[22:23], v[18:19], 0, s[96:97]
	v_lshl_add_u64 v[26:27], v[22:23], 0, s[96:97]
	v_lshl_add_u64 v[40:41], v[26:27], 0, s[96:97]
	global_load_dwordx4 v[2:5], v[6:7], off nt
	v_or_b32_e32 v72, s15, v54
	global_load_dwordx4 v[6:9], v[10:11], off nt
	v_ashrrev_i32_e32 v73, 31, v72
	global_load_dwordx4 v[10:13], v[14:15], off nt
	v_lshlrev_b64 v[72:73], 12, v[72:73]
	global_load_dwordx4 v[14:17], v[18:19], off nt
	v_lshl_add_u64 v[72:73], s[38:39], 0, v[72:73]
	global_load_dwordx4 v[18:21], v[22:23], off nt
	s_ashr_i32 s35, s34, 31
	global_load_dwordx4 v[22:25], v[26:27], off nt
	v_lshl_add_u64 v[72:73], s[34:35], 1, v[72:73]
	global_load_dwordx4 v[26:29], v[40:41], off nt
	v_lshl_add_u64 v[40:41], v[40:41], 0, s[96:97]
	global_load_dwordx4 v[40:43], v[40:41], off nt
	v_lshlrev_b32_e32 v34, 1, v52
	v_lshl_add_u64 v[76:77], v[72:73], 0, v[34:35]
	s_waitcnt vmcnt(0)
	v_cvt_pk_bf16_f32 v72, v30, v36
	v_add_co_u32_e32 v30, vcc, s90, v76
	v_cvt_pk_bf16_f32 v73, v44, v48
	v_cvt_pk_bf16_f32 v74, v56, v60
	v_cvt_pk_bf16_f32 v75, v64, v68
	global_store_dwordx4 v[76:77], v[72:75], off nt
	s_nop 1
	v_cvt_pk_bf16_f32 v72, v31, v37
	v_addc_co_u32_e32 v31, vcc, 0, v77, vcc
	v_cvt_pk_bf16_f32 v73, v45, v49
	v_cvt_pk_bf16_f32 v74, v57, v61
	v_cvt_pk_bf16_f32 v75, v65, v69
	v_add_co_u32_e32 v36, vcc, 0x3000, v76
	global_store_dwordx4 v[30:31], v[72:75], off offset:-4096 nt
	s_nop 0
	v_addc_co_u32_e32 v37, vcc, 0, v77, vcc
	v_cvt_pk_bf16_f32 v72, v32, v38
	v_cvt_pk_bf16_f32 v73, v46, v50
	v_cvt_pk_bf16_f32 v74, v58, v62
	v_cvt_pk_bf16_f32 v75, v66, v70
	global_store_dwordx4 v[30:31], v[72:75], off nt
	v_cvt_pk_bf16_f32 v30, v33, v39
	v_cvt_pk_bf16_f32 v31, v47, v51
	v_cvt_pk_bf16_f32 v32, v59, v63
	v_cvt_pk_bf16_f32 v33, v67, v71
	s_andn2_b64 vcc, exec, s[22:23]
	global_store_dwordx4 v[36:37], v[30:33], off nt
	s_cbranch_vccnz .LBB0_764
	v_add_u32_e32 v1, s14, v54
	v_mad_i64_i32 v[30:31], s[4:5], s28, v1, 0
	v_lshl_add_u64 v[30:31], v[30:31], 1, s[26:27]
	s_ashr_i32 s25, s24, 31
	v_lshl_add_u64 v[30:31], s[24:25], 1, v[30:31]
	v_lshl_add_u64 v[36:37], v[30:31], 0, v[34:35]
	v_cvt_pk_bf16_f32 v30, v2, v6
	v_cvt_pk_bf16_f32 v31, v10, v14
	v_cvt_pk_bf16_f32 v32, v18, v22
	v_cvt_pk_bf16_f32 v33, v26, v40
	s_lshl_b32 s96, s28, 1
	global_store_dwordx4 v[36:37], v[30:33], off nt
	s_nop 1
	v_cvt_pk_bf16_f32 v30, v3, v7
	v_cvt_pk_bf16_f32 v31, v11, v15
	v_cvt_pk_bf16_f32 v32, v19, v23
	v_cvt_pk_bf16_f32 v33, v27, v41
	v_lshl_add_u64 v[2:3], v[36:37], 0, s[96:97]
	global_store_dwordx4 v[2:3], v[30:33], off nt
	v_lshl_add_u64 v[6:7], v[2:3], 0, s[96:97]
	v_cvt_pk_bf16_f32 v2, v5, v9
	v_cvt_pk_bf16_f32 v30, v4, v8
	v_cvt_pk_bf16_f32 v31, v12, v16
	v_cvt_pk_bf16_f32 v32, v20, v24
	v_cvt_pk_bf16_f32 v33, v28, v42
	global_store_dwordx4 v[6:7], v[30:33], off nt
	v_cvt_pk_bf16_f32 v3, v13, v17
	v_cvt_pk_bf16_f32 v4, v21, v25
	v_cvt_pk_bf16_f32 v5, v29, v43
	v_lshl_add_u64 v[6:7], v[6:7], 0, s[96:97]
	global_store_dwordx4 v[6:7], v[2:5], off nt
	s_branch .LBB0_764

.LBB0_918:
	s_ashr_i32 s5, s49, 31
	s_lshr_b32 s5, s5, 18
	s_add_i32 s5, s49, s5
	s_ashr_i32 s15, s5, 14
	s_and_b32 s5, s5, 0xffffc000
	s_sub_i32 s5, s49, s5
	s_sext_i32_i16 s21, s5
	s_lshr_b32 s21, s21, 22
	s_and_b32 s21, s21, 0x1ff
	s_add_i32 s21, s5, s21
	s_sext_i32_i16 s25, s21
	s_and_b32 s21, s21, 0xfe00
	s_sub_i32 s5, s5, s21
	s_sext_i32_i16 s21, s5
	s_bfe_u32 s21, s21, 0x4001b
	s_add_i32 s21, s5, s21
	s_lshr_b32 s28, s25, 9
	s_sext_i32_i16 s25, s21
	s_and_b32 s21, s21, 0xfff0
	s_sub_i32 s5, s5, s21
	s_sext_i32_i16 s5, s5
	s_lshl_b32 s50, s5, 5
	s_cmpk_gt_i32 s49, 0xc000
	s_cselect_b32 s21, s44, s46
	s_cselect_b32 s31, s43, s45
	s_bfe_i64 s[28:29], s[28:29], 0x100000
	s_lshl_b64 s[28:29], s[28:29], 22
	s_add_u32 s52, s31, s28
	s_addc_u32 s53, s21, s29
	s_add_u32 s34, s36, s28
	s_addc_u32 s35, s37, s29
	s_lshl_b32 s5, s5, 6
	s_and_b32 s21, s50, 0x60
	s_lshl_b32 s15, s15, 7
	s_and_b32 s5, s5, 0xffffff00
	s_or_b32 s15, s21, s15
	s_add_i32 s15, s15, s5
	s_lshl_b32 s5, s25, 2
	s_and_b32 s28, s5, 0xffffffc0
	v_or_b32_e32 v2, s28, v52
	v_ashrrev_i32_e32 v3, 31, v2
	v_lshlrev_b64 v[2:3], 11, v[2:3]
	v_lshl_add_u64 v[2:3], s[52:53], 0, v[2:3]
	s_ashr_i32 s51, s50, 31
	v_lshl_add_u64 v[2:3], s[50:51], 2, v[2:3]
	v_lshlrev_b32_e32 v34, 2, v54
	v_lshl_add_u64 v[2:3], v[2:3], 0, v[34:35]
	v_add_co_u32_e32 v4, vcc, s73, v2
	global_load_dwordx4 v[30:33], v[2:3], off nt
	global_load_dwordx4 v[36:39], v[2:3], off offset:2048 nt
	v_addc_co_u32_e32 v5, vcc, 0, v3, vcc
	v_add_co_u32_e32 v6, vcc, s90, v2
	s_ashr_i32 s5, s4, 31
	s_nop 0
	v_addc_co_u32_e32 v7, vcc, 0, v3, vcc
	v_add_co_u32_e32 v2, vcc, s91, v2
	global_load_dwordx4 v[44:47], v[6:7], off offset:-4096 nt
	global_load_dwordx4 v[48:51], v[4:5], off offset:2048 nt
	global_load_dwordx4 v[56:59], v[6:7], off nt
	global_load_dwordx4 v[60:63], v[6:7], off offset:2048 nt
	v_addc_co_u32_e32 v3, vcc, 0, v3, vcc
	global_load_dwordx4 v[64:67], v[2:3], off nt
	global_load_dwordx4 v[68:71], v[2:3], off offset:2048 nt
	v_or_b32_e32 v2, s20, v52
	v_mul_hi_i32_i24_e32 v3, s30, v2
	v_mul_i32_i24_e32 v2, s30, v2
	v_lshl_add_u64 v[2:3], v[2:3], 2, s[26:27]
	v_lshl_add_u64 v[2:3], s[4:5], 2, v[2:3]
	v_lshl_add_u64 v[6:7], v[2:3], 0, v[34:35]
	s_lshl_b32 s96, s30, 2
	v_lshl_add_u64 v[10:11], v[6:7], 0, s[96:97]
	v_lshl_add_u64 v[14:15], v[10:11], 0, s[96:97]
	v_lshl_add_u64 v[18:19], v[14:15], 0, s[96:97]
	v_lshl_add_u64 v[22:23], v[18:19], 0, s[96:97]
	v_lshl_add_u64 v[26:27], v[22:23], 0, s[96:97]
	v_lshl_add_u64 v[40:41], v[26:27], 0, s[96:97]
	global_load_dwordx4 v[2:5], v[6:7], off nt
	v_or_b32_e32 v72, s15, v54
	global_load_dwordx4 v[6:9], v[10:11], off nt
	v_ashrrev_i32_e32 v73, 31, v72
	global_load_dwordx4 v[10:13], v[14:15], off nt
	v_lshlrev_b64 v[72:73], 12, v[72:73]
	global_load_dwordx4 v[14:17], v[18:19], off nt
	v_lshl_add_u64 v[72:73], s[34:35], 0, v[72:73]
	global_load_dwordx4 v[18:21], v[22:23], off nt
	s_ashr_i32 s29, s28, 31
	global_load_dwordx4 v[22:25], v[26:27], off nt
	v_lshl_add_u64 v[72:73], s[28:29], 1, v[72:73]
	global_load_dwordx4 v[26:29], v[40:41], off nt
	v_lshl_add_u64 v[40:41], v[40:41], 0, s[96:97]
	global_load_dwordx4 v[40:43], v[40:41], off nt
	v_lshlrev_b32_e32 v34, 1, v52
	v_lshl_add_u64 v[76:77], v[72:73], 0, v[34:35]
	s_waitcnt vmcnt(0)
	v_cvt_pk_bf16_f32 v72, v30, v36
	v_add_co_u32_e32 v30, vcc, s90, v76
	v_cvt_pk_bf16_f32 v73, v44, v48
	v_cvt_pk_bf16_f32 v74, v56, v60
	v_cvt_pk_bf16_f32 v75, v64, v68
	global_store_dwordx4 v[76:77], v[72:75], off nt
	s_nop 1
	v_cvt_pk_bf16_f32 v72, v31, v37
	v_addc_co_u32_e32 v31, vcc, 0, v77, vcc
	v_cvt_pk_bf16_f32 v73, v45, v49
	v_cvt_pk_bf16_f32 v74, v57, v61
	v_cvt_pk_bf16_f32 v75, v65, v69
	v_add_co_u32_e32 v36, vcc, 0x3000, v76
	global_store_dwordx4 v[30:31], v[72:75], off offset:-4096 nt
	s_nop 0
	v_addc_co_u32_e32 v37, vcc, 0, v77, vcc
	v_cvt_pk_bf16_f32 v72, v32, v38
	v_cvt_pk_bf16_f32 v73, v46, v50
	v_cvt_pk_bf16_f32 v74, v58, v62
	v_cvt_pk_bf16_f32 v75, v66, v70
	global_store_dwordx4 v[30:31], v[72:75], off nt
	v_cvt_pk_bf16_f32 v30, v33, v39
	v_cvt_pk_bf16_f32 v31, v47, v51
	v_cvt_pk_bf16_f32 v32, v59, v63
	v_cvt_pk_bf16_f32 v33, v67, v71
	s_andn2_b64 vcc, exec, s[18:19]
	global_store_dwordx4 v[36:37], v[30:33], off nt
	s_cbranch_vccnz .LBB0_912
	s_nop 0
	v_add_u32_e32 v30, s14, v54
	v_mad_i64_i32 v[30:31], s[4:5], s24, v30, 0
	v_lshl_add_u64 v[30:31], v[30:31], 1, s[22:23]
	s_ashr_i32 s21, s20, 31
	v_lshl_add_u64 v[30:31], s[20:21], 1, v[30:31]
	v_lshl_add_u64 v[36:37], v[30:31], 0, v[34:35]
	v_cvt_pk_bf16_f32 v30, v2, v6
	v_cvt_pk_bf16_f32 v31, v10, v14
	v_cvt_pk_bf16_f32 v32, v18, v22
	v_cvt_pk_bf16_f32 v33, v26, v40
	s_lshl_b32 s96, s24, 1
	global_store_dwordx4 v[36:37], v[30:33], off nt
	s_nop 1
	v_cvt_pk_bf16_f32 v30, v3, v7
	v_cvt_pk_bf16_f32 v31, v11, v15
	v_cvt_pk_bf16_f32 v32, v19, v23
	v_cvt_pk_bf16_f32 v33, v27, v41
	v_lshl_add_u64 v[2:3], v[36:37], 0, s[96:97]
	global_store_dwordx4 v[2:3], v[30:33], off nt
	v_lshl_add_u64 v[6:7], v[2:3], 0, s[96:97]
	v_cvt_pk_bf16_f32 v2, v5, v9
	v_cvt_pk_bf16_f32 v30, v4, v8
	v_cvt_pk_bf16_f32 v31, v12, v16
	v_cvt_pk_bf16_f32 v32, v20, v24
	v_cvt_pk_bf16_f32 v33, v28, v42
	global_store_dwordx4 v[6:7], v[30:33], off nt
	v_cvt_pk_bf16_f32 v3, v13, v17
	v_cvt_pk_bf16_f32 v4, v21, v25
	v_cvt_pk_bf16_f32 v5, v29, v43
	v_lshl_add_u64 v[6:7], v[6:7], 0, s[96:97]
	global_store_dwordx4 v[6:7], v[2:5], off nt
	s_branch .LBB0_912

.LBB0_931:
	s_ashr_i32 s5, s41, 31
	s_lshr_b32 s5, s5, 18
	s_add_i32 s5, s41, s5
	s_ashr_i32 s15, s5, 14
	s_and_b32 s5, s5, 0xffffc000
	s_sub_i32 s5, s41, s5
	s_sext_i32_i16 s21, s5
	s_lshr_b32 s21, s21, 22
	s_and_b32 s21, s21, 0x1ff
	s_add_i32 s21, s5, s21
	s_sext_i32_i16 s25, s21
	s_and_b32 s21, s21, 0xfe00
	s_sub_i32 s5, s5, s21
	s_sext_i32_i16 s21, s5
	s_bfe_u32 s21, s21, 0x4001b
	s_add_i32 s21, s5, s21
	s_lshr_b32 s28, s25, 9
	s_sext_i32_i16 s25, s21
	s_and_b32 s21, s21, 0xfff0
	s_sub_i32 s5, s5, s21
	s_sext_i32_i16 s5, s5
	s_lshl_b32 s50, s5, 5
	s_cmpk_gt_i32 s41, 0xc000
	s_cselect_b32 s21, s43, s45
	s_cselect_b32 s31, s42, s44
	s_bfe_i64 s[28:29], s[28:29], 0x100000
	s_lshl_b64 s[28:29], s[28:29], 22
	s_add_u32 s52, s31, s28
	s_addc_u32 s53, s21, s29
	s_add_u32 s34, s36, s28
	s_addc_u32 s35, s37, s29
	s_lshl_b32 s5, s5, 6
	s_and_b32 s21, s50, 0x60
	s_lshl_b32 s15, s15, 7
	s_and_b32 s5, s5, 0xffffff00
	s_or_b32 s15, s21, s15
	s_add_i32 s15, s15, s5
	s_lshl_b32 s5, s25, 2
	s_and_b32 s28, s5, 0xffffffc0
	v_or_b32_e32 v2, s28, v52
	v_ashrrev_i32_e32 v3, 31, v2
	v_lshlrev_b64 v[2:3], 11, v[2:3]
	v_lshl_add_u64 v[2:3], s[52:53], 0, v[2:3]
	s_ashr_i32 s51, s50, 31
	v_lshl_add_u64 v[2:3], s[50:51], 2, v[2:3]
	v_lshlrev_b32_e32 v34, 2, v54
	v_lshl_add_u64 v[2:3], v[2:3], 0, v[34:35]
	v_add_co_u32_e32 v4, vcc, s73, v2
	global_load_dwordx4 v[30:33], v[2:3], off nt
	global_load_dwordx4 v[36:39], v[2:3], off offset:2048 nt
	v_addc_co_u32_e32 v5, vcc, 0, v3, vcc
	v_add_co_u32_e32 v6, vcc, s90, v2
	v_or_b32_e32 v1, s20, v52
	s_nop 0
	v_addc_co_u32_e32 v7, vcc, 0, v3, vcc
	v_add_co_u32_e32 v2, vcc, s91, v2
	global_load_dwordx4 v[44:47], v[6:7], off offset:-4096 nt
	global_load_dwordx4 v[48:51], v[4:5], off offset:2048 nt
	global_load_dwordx4 v[56:59], v[6:7], off nt
	global_load_dwordx4 v[60:63], v[6:7], off offset:2048 nt
	v_addc_co_u32_e32 v3, vcc, 0, v3, vcc
	global_load_dwordx4 v[64:67], v[2:3], off nt
	global_load_dwordx4 v[68:71], v[2:3], off offset:2048 nt
	v_mul_hi_i32_i24_e32 v3, s30, v1
	v_mul_i32_i24_e32 v2, s30, v1
	v_lshl_add_u64 v[2:3], v[2:3], 2, s[26:27]
	s_ashr_i32 s5, s4, 31
	v_lshl_add_u64 v[2:3], s[4:5], 2, v[2:3]
	v_lshl_add_u64 v[6:7], v[2:3], 0, v[34:35]
	s_lshl_b32 s96, s30, 2
	v_lshl_add_u64 v[10:11], v[6:7], 0, s[96:97]
	v_lshl_add_u64 v[14:15], v[10:11], 0, s[96:97]
	v_lshl_add_u64 v[18:19], v[14:15], 0, s[96:97]
	v_lshl_add_u64 v[22:23], v[18:19], 0, s[96:97]
	v_lshl_add_u64 v[26:27], v[22:23], 0, s[96:97]
	v_lshl_add_u64 v[40:41], v[26:27], 0, s[96:97]
	global_load_dwordx4 v[2:5], v[6:7], off nt
	v_or_b32_e32 v72, s15, v54
	global_load_dwordx4 v[6:9], v[10:11], off nt
	v_ashrrev_i32_e32 v73, 31, v72
	global_load_dwordx4 v[10:13], v[14:15], off nt
	v_lshlrev_b64 v[72:73], 12, v[72:73]
	global_load_dwordx4 v[14:17], v[18:19], off nt
	v_lshl_add_u64 v[72:73], s[34:35], 0, v[72:73]
	global_load_dwordx4 v[18:21], v[22:23], off nt
	s_ashr_i32 s29, s28, 31
	global_load_dwordx4 v[22:25], v[26:27], off nt
	v_lshl_add_u64 v[72:73], s[28:29], 1, v[72:73]
	global_load_dwordx4 v[26:29], v[40:41], off nt
	v_lshl_add_u64 v[40:41], v[40:41], 0, s[96:97]
	global_load_dwordx4 v[40:43], v[40:41], off nt
	v_lshlrev_b32_e32 v34, 1, v52
	v_lshl_add_u64 v[76:77], v[72:73], 0, v[34:35]
	s_waitcnt vmcnt(0)
	v_cvt_pk_bf16_f32 v72, v30, v36
	v_add_co_u32_e32 v30, vcc, s90, v76
	v_cvt_pk_bf16_f32 v73, v44, v48
	v_cvt_pk_bf16_f32 v74, v56, v60
	v_cvt_pk_bf16_f32 v75, v64, v68
	global_store_dwordx4 v[76:77], v[72:75], off nt
	s_nop 1
	v_cvt_pk_bf16_f32 v72, v31, v37
	v_addc_co_u32_e32 v31, vcc, 0, v77, vcc
	v_cvt_pk_bf16_f32 v73, v45, v49
	v_cvt_pk_bf16_f32 v74, v57, v61
	v_cvt_pk_bf16_f32 v75, v65, v69
	v_add_co_u32_e32 v36, vcc, 0x3000, v76
	global_store_dwordx4 v[30:31], v[72:75], off offset:-4096 nt
	s_nop 0
	v_addc_co_u32_e32 v37, vcc, 0, v77, vcc
	v_cvt_pk_bf16_f32 v72, v32, v38
	v_cvt_pk_bf16_f32 v73, v46, v50
	v_cvt_pk_bf16_f32 v74, v58, v62
	v_cvt_pk_bf16_f32 v75, v66, v70
	global_store_dwordx4 v[30:31], v[72:75], off nt
	v_cvt_pk_bf16_f32 v30, v33, v39
	v_cvt_pk_bf16_f32 v31, v47, v51
	v_cvt_pk_bf16_f32 v32, v59, v63
	v_cvt_pk_bf16_f32 v33, v67, v71
	s_andn2_b64 vcc, exec, s[18:19]
	global_store_dwordx4 v[36:37], v[30:33], off nt
	s_cbranch_vccnz .LBB0_925
	v_add_u32_e32 v1, s14, v54
	v_mad_i64_i32 v[30:31], s[4:5], s24, v1, 0
	v_lshl_add_u64 v[30:31], v[30:31], 1, s[22:23]
	s_ashr_i32 s21, s20, 31
	v_lshl_add_u64 v[30:31], s[20:21], 1, v[30:31]
	v_lshl_add_u64 v[36:37], v[30:31], 0, v[34:35]
	v_cvt_pk_bf16_f32 v30, v2, v6
	v_cvt_pk_bf16_f32 v31, v10, v14
	v_cvt_pk_bf16_f32 v32, v18, v22
	v_cvt_pk_bf16_f32 v33, v26, v40
	s_lshl_b32 s96, s24, 1
	global_store_dwordx4 v[36:37], v[30:33], off nt
	s_nop 1
	v_cvt_pk_bf16_f32 v30, v3, v7
	v_cvt_pk_bf16_f32 v31, v11, v15
	v_cvt_pk_bf16_f32 v32, v19, v23
	v_cvt_pk_bf16_f32 v33, v27, v41
	v_lshl_add_u64 v[2:3], v[36:37], 0, s[96:97]
	global_store_dwordx4 v[2:3], v[30:33], off nt
	v_lshl_add_u64 v[6:7], v[2:3], 0, s[96:97]
	v_cvt_pk_bf16_f32 v2, v5, v9
	v_cvt_pk_bf16_f32 v30, v4, v8
	v_cvt_pk_bf16_f32 v31, v12, v16
	v_cvt_pk_bf16_f32 v32, v20, v24
	v_cvt_pk_bf16_f32 v33, v28, v42
	global_store_dwordx4 v[6:7], v[30:33], off nt
	v_cvt_pk_bf16_f32 v3, v13, v17
	v_cvt_pk_bf16_f32 v4, v21, v25
	v_cvt_pk_bf16_f32 v5, v29, v43
	v_lshl_add_u64 v[6:7], v[6:7], 0, s[96:97]
	global_store_dwordx4 v[6:7], v[2:5], off nt
	s_branch .LBB0_925

.LBB0_1119:
	v_or_b32_e32 v1, s26, v36
	v_mul_hi_i32_i24_e32 v3, s34, v1
	v_mul_i32_i24_e32 v2, s34, v1
	v_lshl_add_u64 v[2:3], v[2:3], 2, s[30:31]
	s_ashr_i32 s5, s4, 31
	v_lshl_add_u64 v[2:3], s[4:5], 2, v[2:3]
	v_lshlrev_b32_e32 v34, 2, v38
	v_lshl_add_u64 v[2:3], v[2:3], 0, v[34:35]
	s_lshl_b32 s96, s34, 2
	global_load_dwordx4 v[40:43], v[2:3], off nt
	v_lshl_add_u64 v[2:3], v[2:3], 0, s[96:97]
	global_load_dwordx4 v[44:47], v[2:3], off nt
	v_lshl_add_u64 v[2:3], v[2:3], 0, s[96:97]
	global_load_dwordx4 v[48:51], v[2:3], off nt
	v_lshl_add_u64 v[2:3], v[2:3], 0, s[96:97]
	global_load_dwordx4 v[52:55], v[2:3], off nt
	v_lshl_add_u64 v[2:3], v[2:3], 0, s[96:97]
	global_load_dwordx4 v[56:59], v[2:3], off nt
	v_lshl_add_u64 v[2:3], v[2:3], 0, s[96:97]
	global_load_dwordx4 v[60:63], v[2:3], off nt
	v_lshl_add_u64 v[2:3], v[2:3], 0, s[96:97]
	global_load_dwordx4 v[64:67], v[2:3], off nt
	v_lshl_add_u64 v[2:3], v[2:3], 0, s[96:97]
	v_or_b32_e32 v1, s18, v36
	global_load_dwordx4 v[68:71], v[2:3], off nt
	v_mul_hi_i32_i24_e32 v3, s14, v1
	v_mul_i32_i24_e32 v2, s14, v1
	v_lshl_add_u64 v[2:3], v[2:3], 2, s[38:39]
	s_ashr_i32 s37, s36, 31
	v_lshl_add_u64 v[2:3], s[36:37], 2, v[2:3]
	v_lshl_add_u64 v[6:7], v[2:3], 0, v[34:35]
	s_lshl_b32 s96, s14, 2
	v_lshl_add_u64 v[10:11], v[6:7], 0, s[96:97]
	v_lshl_add_u64 v[14:15], v[10:11], 0, s[96:97]
	v_lshl_add_u64 v[18:19], v[14:15], 0, s[96:97]
	v_lshl_add_u64 v[22:23], v[18:19], 0, s[96:97]
	v_lshl_add_u64 v[26:27], v[22:23], 0, s[96:97]
	v_lshl_add_u64 v[30:31], v[26:27], 0, s[96:97]
	global_load_dwordx4 v[2:5], v[6:7], off nt
	v_add_u32_e32 v1, s27, v38
	global_load_dwordx4 v[6:9], v[10:11], off nt
	v_mad_i64_i32 v[72:73], s[4:5], s24, v1, 0
	global_load_dwordx4 v[10:13], v[14:15], off nt
	v_lshl_add_u64 v[72:73], v[72:73], 1, s[28:29]
	global_load_dwordx4 v[14:17], v[18:19], off nt
	s_ashr_i32 s27, s26, 31
	global_load_dwordx4 v[18:21], v[22:23], off nt
	v_lshl_add_u64 v[72:73], s[26:27], 1, v[72:73]
	global_load_dwordx4 v[22:25], v[26:27], off nt
	v_lshlrev_b32_e32 v34, 1, v36
	global_load_dwordx4 v[26:29], v[30:31], off nt
	v_lshl_add_u64 v[30:31], v[30:31], 0, s[96:97]
	global_load_dwordx4 v[30:33], v[30:31], off nt
	v_lshl_add_u64 v[76:77], v[72:73], 0, v[34:35]
	s_lshl_b32 s96, s24, 1
	s_andn2_b64 vcc, exec, s[16:17]
	s_waitcnt vmcnt(0)
	v_cvt_pk_bf16_f32 v72, v40, v44
	v_cvt_pk_bf16_f32 v73, v48, v52
	v_cvt_pk_bf16_f32 v74, v56, v60
	v_cvt_pk_bf16_f32 v75, v64, v68
	global_store_dwordx4 v[76:77], v[72:75], off nt
	s_nop 1
	v_cvt_pk_bf16_f32 v72, v41, v45
	v_cvt_pk_bf16_f32 v73, v49, v53
	v_cvt_pk_bf16_f32 v74, v57, v61
	v_cvt_pk_bf16_f32 v75, v65, v69
	v_lshl_add_u64 v[40:41], v[76:77], 0, s[96:97]
	global_store_dwordx4 v[40:41], v[72:75], off nt
	v_lshl_add_u64 v[44:45], v[40:41], 0, s[96:97]
	v_cvt_pk_bf16_f32 v40, v43, v47
	v_cvt_pk_bf16_f32 v72, v42, v46
	v_cvt_pk_bf16_f32 v73, v50, v54
	v_cvt_pk_bf16_f32 v74, v58, v62
	v_cvt_pk_bf16_f32 v75, v66, v70
	global_store_dwordx4 v[44:45], v[72:75], off nt
	v_cvt_pk_bf16_f32 v41, v51, v55
	v_cvt_pk_bf16_f32 v42, v59, v63
	v_cvt_pk_bf16_f32 v43, v67, v71
	v_lshl_add_u64 v[44:45], v[44:45], 0, s[96:97]
	global_store_dwordx4 v[44:45], v[40:43], off nt
	s_cbranch_vccnz .LBB0_1108
	v_add_u32_e32 v1, s19, v38
	v_mad_i64_i32 v[40:41], s[4:5], s22, v1, 0
	v_lshl_add_u64 v[40:41], v[40:41], 1, s[20:21]
	s_ashr_i32 s19, s18, 31
	v_lshl_add_u64 v[40:41], s[18:19], 1, v[40:41]
	v_lshl_add_u64 v[44:45], v[40:41], 0, v[34:35]
	v_cvt_pk_bf16_f32 v40, v2, v6
	v_cvt_pk_bf16_f32 v41, v10, v14
	v_cvt_pk_bf16_f32 v42, v18, v22
	v_cvt_pk_bf16_f32 v43, v26, v30
	s_lshl_b32 s96, s22, 1
	global_store_dwordx4 v[44:45], v[40:43], off nt
	s_nop 1
	v_cvt_pk_bf16_f32 v40, v3, v7
	v_cvt_pk_bf16_f32 v41, v11, v15
	v_cvt_pk_bf16_f32 v42, v19, v23
	v_cvt_pk_bf16_f32 v43, v27, v31
	v_lshl_add_u64 v[2:3], v[44:45], 0, s[96:97]
	global_store_dwordx4 v[2:3], v[40:43], off nt
	v_lshl_add_u64 v[6:7], v[2:3], 0, s[96:97]
	v_cvt_pk_bf16_f32 v2, v5, v9
	v_cvt_pk_bf16_f32 v40, v4, v8
	v_cvt_pk_bf16_f32 v41, v12, v16
	v_cvt_pk_bf16_f32 v42, v20, v24
	v_cvt_pk_bf16_f32 v43, v28, v32
	global_store_dwordx4 v[6:7], v[40:43], off nt
	v_cvt_pk_bf16_f32 v3, v13, v17
	v_cvt_pk_bf16_f32 v4, v21, v25
	v_cvt_pk_bf16_f32 v5, v29, v33
	v_lshl_add_u64 v[6:7], v[6:7], 0, s[96:97]
	global_store_dwordx4 v[6:7], v[2:5], off nt
	s_branch .LBB0_1108
